# baseline (speedup 1.0000x reference)
.LBB1_6:
	s_and_b32 s16, s2, 7
	s_mul_i32 s0, s16, 0x4b
	s_add_i32 s22, s3, s0
	s_lshr_b32 s23, s25, 6
	s_cmp_ge_u32 s23, s14
	s_cselect_b64 s[0:1], -1, 0
	s_cmp_lt_u32 s23, s15
	s_cselect_b64 s[2:3], -1, 0
	s_and_b64 s[8:9], s[0:1], s[2:3]
	s_mul_i32 s16, s16, 5
	s_add_i32 s24, s23, s16
	s_waitcnt lgkmcnt(0)
	s_mul_i32 s2, s22, 0x28000
	s_mul_hi_u32 s1, s22, 0x28000
	s_add_u32 s2, s4, s2
	s_addc_u32 s3, s5, s1
	s_mul_i32 s4, s24, 0x14000
	s_add_u32 s4, s6, s4
	s_addc_u32 s5, s7, 0
	s_add_u32 s4, s4, 0x32000
	s_addc_u32 s5, s5, 0
	s_movk_i32 s0, 0xc0
	v_cmp_gt_u32_e64 s[16:17], s0, v0
	v_lshlrev_b32_e32 v118, 4, v0
	v_add_u32_e32 v119, 0x1400, v118
	v_and_b32_e32 v65, 63, v0
	v_lshlrev_b32_e32 v120, 4, v65
	v_cndmask_b32_e64 v119, v118, v119, s[16:17]
	s_lshl_b32 s28, s23, 12
	v_add_u32_e32 v121, s28, v120
	s_add_i32 s28, s28, 10240
	s_lshl_b32 s29, s23, 10
	s_add_i32 s30, s29, 38912
	s_add_i32 s29, s29, 30720
	s_add_i32 s31, s29, 5120
	s_add_i32 s32, s30, 5120
	s_cmp_lt_u32 s23, 3
	s_cbranch_scc1 .Lg_m0ok
	s_lshl_b32 s31, s23, 10
	s_add_i32 s31, s31, 44032
	s_mov_b32 s32, s31
.Lg_m0ok:
	v_bfe_u32 v2, v0, 2, 4
	v_mul_u32_u24_e32 v2, 0xa0, v2
	v_lshlrev_b32_e32 v6, 3, v0
	v_and_or_b32 v108, v6, 24, v2
	v_lshrrev_b32_e32 v1, 4, v0
	v_mul_u32_u24_e32 v2, 0xa0, v1
	v_and_b32_e32 v3, 0x78, v6
	v_add_u32_e32 v109, v2, v3
	s_mov_b32 m0, s29
	s_nop 0
	global_load_lds_dwordx4 v118, s[2:3] nt
	s_mov_b32 m0, s31
	s_nop 0
	global_load_lds_dwordx4 v119, s[2:3] nt
	s_mov_b32 m0, s28
	s_nop 0
	global_load_lds_dwordx4 v120, s[4:5]
	global_load_lds_dwordx4 v120, s[4:5] offset:1024
	global_load_lds_dwordx4 v120, s[4:5] offset:2048
	global_load_lds_dwordx4 v120, s[4:5] offset:3072
	s_add_u32 s36, s2, 0x2000
	s_addc_u32 s37, s3, 0
	s_mov_b32 m0, s30
	s_nop 0
	global_load_lds_dwordx4 v118, s[36:37] nt
	s_mov_b32 m0, s32
	s_nop 0
	global_load_lds_dwordx4 v119, s[36:37] nt
	v_mov_b32_e32 v0, 0
	v_mov_b32_e32 v1, 0
	v_mov_b64_e32 v[2:3], v[0:1]
	v_mov_b64_e32 v[4:5], v[0:1]
	v_mov_b64_e32 v[6:7], v[0:1]
	v_mov_b64_e32 v[8:9], v[0:1]
	v_mov_b64_e32 v[10:11], v[0:1]
	v_mov_b64_e32 v[12:13], v[0:1]
	v_mov_b64_e32 v[14:15], v[0:1]
	v_mov_b64_e32 v[16:17], v[0:1]
	v_mov_b64_e32 v[18:19], v[0:1]
	v_mov_b64_e32 v[20:21], v[0:1]
	v_mov_b64_e32 v[22:23], v[0:1]
	v_mov_b64_e32 v[24:25], v[0:1]
	v_mov_b64_e32 v[26:27], v[0:1]
	v_mov_b64_e32 v[28:29], v[0:1]
	v_mov_b64_e32 v[30:31], v[0:1]
	v_mov_b64_e32 v[32:33], v[0:1]
	v_mov_b64_e32 v[34:35], v[0:1]
	v_mov_b64_e32 v[36:37], v[0:1]
	v_mov_b64_e32 v[38:39], v[0:1]
	v_mov_b64_e32 v[40:41], v[0:1]
	v_mov_b64_e32 v[42:43], v[0:1]
	v_mov_b64_e32 v[44:45], v[0:1]
	v_mov_b64_e32 v[46:47], v[0:1]
	v_mov_b64_e32 v[48:49], v[0:1]
	v_mov_b64_e32 v[50:51], v[0:1]
	v_mov_b64_e32 v[52:53], v[0:1]
	v_mov_b64_e32 v[54:55], v[0:1]
	v_mov_b64_e32 v[56:57], v[0:1]
	v_mov_b64_e32 v[58:59], v[0:1]
	v_mov_b64_e32 v[60:61], v[0:1]
	v_mov_b64_e32 v[62:63], v[0:1]
	v_mov_b64_e32 v[104:105], v[0:1]
	v_mov_b64_e32 v[106:107], v[0:1]
	s_mov_b32 s26, 0
.Lg_loop:
	s_waitcnt vmcnt(2)
	ds_read_b128 v[68:71], v118 offset:30720
	ds_read_b128 v[64:67], v118 offset:35840
	ds_read_b128 v[80:83], v121 offset:10240
	ds_read_b128 v[84:87], v121 offset:11264
	ds_read_b128 v[88:91], v121 offset:12288
	ds_read_b128 v[92:95], v121 offset:13312
	s_add_i32 s33, s26, 1
	s_min_u32 s33, s33, 19
	s_lshl_b32 s33, s33, 12
	s_add_u32 s38, s4, s33
	s_addc_u32 s39, s5, 0
	s_add_i32 s33, s26, 2
	s_min_u32 s33, s33, 19
	s_lshl_b32 s33, s33, 13
	s_add_u32 s36, s2, s33
	s_addc_u32 s37, s3, 0
	s_waitcnt lgkmcnt(0)
	s_mov_b32 m0, s28
	s_nop 0
	global_load_lds_dwordx4 v120, s[38:39]
	global_load_lds_dwordx4 v120, s[38:39] offset:1024
	global_load_lds_dwordx4 v120, s[38:39] offset:2048
	global_load_lds_dwordx4 v120, s[38:39] offset:3072
	s_mov_b32 m0, s29
	s_nop 0
	global_load_lds_dwordx4 v118, s[36:37] nt
	s_mov_b32 m0, s31
	s_nop 0
	global_load_lds_dwordx4 v119, s[36:37] nt
	v_pk_fma_f32 v[104:105], v[68:69], v[68:69], v[104:105]
	v_pk_fma_f32 v[106:107], v[70:71], v[70:71], v[106:107]
	v_cvt_pk_f16_f32 v71, v70, v71
	v_cvt_pk_f16_f32 v70, v68, v69
	ds_write_b64 v109, v[70:71]
	s_and_saveexec_b64 s[40:41], s[16:17]
	v_pk_fma_f32 v[104:105], v[64:65], v[64:65], v[104:105]
	v_pk_fma_f32 v[106:107], v[66:67], v[66:67], v[106:107]
	v_cvt_pk_f16_f32 v67, v66, v67
	v_cvt_pk_f16_f32 v66, v64, v65
	ds_write_b64 v109, v[66:67] offset:3200
	s_mov_b64 exec, s[40:41]
	s_and_b64 vcc, exec, s[8:9]
	s_waitcnt lgkmcnt(0)
	s_barrier
	s_cbranch_vccz .Lg_skip0
	ds_read_b64_tr_b16 v[66:67], v108 offset:2560
	ds_read_b64_tr_b16 v[64:65], v108
	ds_read_b64_tr_b16 v[68:69], v108 offset:32
	ds_read_b64_tr_b16 v[110:111], v108 offset:64
	ds_read_b64_tr_b16 v[114:115], v108 offset:96
	ds_read_b64_tr_b16 v[70:71], v108 offset:2592
	ds_read_b64_tr_b16 v[112:113], v108 offset:2624
	ds_read_b64_tr_b16 v[116:117], v108 offset:2656
	s_waitcnt lgkmcnt(6)
	v_mfma_f32_16x16x32_f16 v[60:63], v[64:67], v[80:83], v[60:63]
	v_mfma_f32_16x16x32_f16 v[56:59], v[64:67], v[84:87], v[56:59]
	v_mfma_f32_16x16x32_f16 v[52:55], v[64:67], v[88:91], v[52:55]
	v_mfma_f32_16x16x32_f16 v[48:51], v[64:67], v[92:95], v[48:51]
	s_waitcnt lgkmcnt(2)
	v_mfma_f32_16x16x32_f16 v[44:47], v[68:71], v[80:83], v[44:47]
	v_mfma_f32_16x16x32_f16 v[40:43], v[68:71], v[84:87], v[40:43]
	v_mfma_f32_16x16x32_f16 v[36:39], v[68:71], v[88:91], v[36:39]
	v_mfma_f32_16x16x32_f16 v[32:35], v[68:71], v[92:95], v[32:35]
	s_waitcnt lgkmcnt(1)
	v_mfma_f32_16x16x32_f16 v[28:31], v[110:113], v[80:83], v[28:31]
	v_mfma_f32_16x16x32_f16 v[24:27], v[110:113], v[84:87], v[24:27]
	v_mfma_f32_16x16x32_f16 v[20:23], v[110:113], v[88:91], v[20:23]
	v_mfma_f32_16x16x32_f16 v[16:19], v[110:113], v[92:95], v[16:19]
	s_waitcnt lgkmcnt(0)
	v_mfma_f32_16x16x32_f16 v[12:15], v[114:117], v[80:83], v[12:15]
	v_mfma_f32_16x16x32_f16 v[8:11], v[114:117], v[84:87], v[8:11]
	v_mfma_f32_16x16x32_f16 v[4:7], v[114:117], v[88:91], v[4:7]
	v_mfma_f32_16x16x32_f16 v[0:3], v[114:117], v[92:95], v[0:3]
.Lg_skip0:
	s_add_i32 s26, s26, 1
	s_waitcnt vmcnt(2)
	ds_read_b128 v[68:71], v118 offset:38912
	ds_read_b128 v[64:67], v118 offset:44032
	ds_read_b128 v[80:83], v121 offset:10240
	ds_read_b128 v[84:87], v121 offset:11264
	ds_read_b128 v[88:91], v121 offset:12288
	ds_read_b128 v[92:95], v121 offset:13312
	s_add_i32 s33, s26, 1
	s_min_u32 s33, s33, 19
	s_lshl_b32 s33, s33, 12
	s_add_u32 s38, s4, s33
	s_addc_u32 s39, s5, 0
	s_add_i32 s33, s26, 2
	s_min_u32 s33, s33, 19
	s_lshl_b32 s33, s33, 13
	s_add_u32 s36, s2, s33
	s_addc_u32 s37, s3, 0
	s_waitcnt lgkmcnt(0)
	s_mov_b32 m0, s28
	s_nop 0
	global_load_lds_dwordx4 v120, s[38:39]
	global_load_lds_dwordx4 v120, s[38:39] offset:1024
	global_load_lds_dwordx4 v120, s[38:39] offset:2048
	global_load_lds_dwordx4 v120, s[38:39] offset:3072
	s_mov_b32 m0, s30
	s_nop 0
	global_load_lds_dwordx4 v118, s[36:37] nt
	s_mov_b32 m0, s32
	s_nop 0
	global_load_lds_dwordx4 v119, s[36:37] nt
	v_pk_fma_f32 v[104:105], v[68:69], v[68:69], v[104:105]
	v_pk_fma_f32 v[106:107], v[70:71], v[70:71], v[106:107]
	v_cvt_pk_f16_f32 v71, v70, v71
	v_cvt_pk_f16_f32 v70, v68, v69
	ds_write_b64 v109, v[70:71] offset:5120
	s_and_saveexec_b64 s[40:41], s[16:17]
	v_pk_fma_f32 v[104:105], v[64:65], v[64:65], v[104:105]
	v_pk_fma_f32 v[106:107], v[66:67], v[66:67], v[106:107]
	v_cvt_pk_f16_f32 v67, v66, v67
	v_cvt_pk_f16_f32 v66, v64, v65
	ds_write_b64 v109, v[66:67] offset:8320
	s_mov_b64 exec, s[40:41]
	s_and_b64 vcc, exec, s[8:9]
	s_waitcnt lgkmcnt(0)
	s_barrier
	s_cbranch_vccz .Lg_skip1
	ds_read_b64_tr_b16 v[66:67], v108 offset:7680
	ds_read_b64_tr_b16 v[64:65], v108 offset:5120
	ds_read_b64_tr_b16 v[68:69], v108 offset:5152
	ds_read_b64_tr_b16 v[110:111], v108 offset:5184
	ds_read_b64_tr_b16 v[114:115], v108 offset:5216
	ds_read_b64_tr_b16 v[70:71], v108 offset:7712
	ds_read_b64_tr_b16 v[112:113], v108 offset:7744
	ds_read_b64_tr_b16 v[116:117], v108 offset:7776
	s_waitcnt lgkmcnt(6)
	v_mfma_f32_16x16x32_f16 v[60:63], v[64:67], v[80:83], v[60:63]
	v_mfma_f32_16x16x32_f16 v[56:59], v[64:67], v[84:87], v[56:59]
	v_mfma_f32_16x16x32_f16 v[52:55], v[64:67], v[88:91], v[52:55]
	v_mfma_f32_16x16x32_f16 v[48:51], v[64:67], v[92:95], v[48:51]
	s_waitcnt lgkmcnt(2)
	v_mfma_f32_16x16x32_f16 v[44:47], v[68:71], v[80:83], v[44:47]
	v_mfma_f32_16x16x32_f16 v[40:43], v[68:71], v[84:87], v[40:43]
	v_mfma_f32_16x16x32_f16 v[36:39], v[68:71], v[88:91], v[36:39]
	v_mfma_f32_16x16x32_f16 v[32:35], v[68:71], v[92:95], v[32:35]
	s_waitcnt lgkmcnt(1)
	v_mfma_f32_16x16x32_f16 v[28:31], v[110:113], v[80:83], v[28:31]
	v_mfma_f32_16x16x32_f16 v[24:27], v[110:113], v[84:87], v[24:27]
	v_mfma_f32_16x16x32_f16 v[20:23], v[110:113], v[88:91], v[20:23]
	v_mfma_f32_16x16x32_f16 v[16:19], v[110:113], v[92:95], v[16:19]
	s_waitcnt lgkmcnt(0)
	v_mfma_f32_16x16x32_f16 v[12:15], v[114:117], v[80:83], v[12:15]
	v_mfma_f32_16x16x32_f16 v[8:11], v[114:117], v[84:87], v[8:11]
	v_mfma_f32_16x16x32_f16 v[4:7], v[114:117], v[88:91], v[4:7]
	v_mfma_f32_16x16x32_f16 v[0:3], v[114:117], v[92:95], v[0:3]
.Lg_skip1:
	s_add_i32 s26, s26, 1
	s_cmp_lt_u32 s26, 20
	s_cbranch_scc1 .Lg_loop
